# speedup vs baseline: 1.0073x; 1.0059x over previous
.LBB0_219:
	s_or_b64 exec, exec, s[8:9]
	s_movk_i32 s40, 3
.Lsafe_fold:
	s_sleep 127
	s_sub_u32 s40, s40, 1
	s_cmp_lg_u32 s40, 0
	s_cbranch_scc1 .Lsafe_fold
	s_cmp_lt_i32 s82, 32
	s_cselect_b64 s[16:17], -1, 0
	s_ashr_i32 s64, s82, 1
	s_lshl_b32 s4, s64, 18
	s_and_b32 s8, s4, 0xc0000
	s_lshl_b32 s4, s64, 6
	s_mov_b64 s[6:7], s[84:85]
	s_and_b32 s65, s82, 1
	s_and_b32 s9, s4, 0xffffff00
	s_load_dwordx2 s[4:5], s[6:7], 0x100
	s_lshl_b32 s10, s65, 17
	s_ashr_i32 s11, s9, 31
	s_add_u32 s8, s8, s9
	s_addc_u32 s9, 0, s11
	s_lshl_b64 s[14:15], s[8:9], 1
	s_waitcnt lgkmcnt(0)
	s_add_u32 s62, s4, 0x198000
	s_addc_u32 s63, s5, 0
	s_add_u32 s8, s62, s10
	s_addc_u32 s9, s63, 0
	s_add_u32 s12, s8, 0x10000
	s_addc_u32 s13, s9, 0
	s_mov_b32 s18, s86
	v_mbcnt_hi_u32_b32 v1, -1, v132
	s_add_u32 s10, s8, 0x80
	s_addc_u32 s11, s9, 0
	v_lshl_add_u32 v2, s18, 6, v1
	s_and_b64 vcc, exec, s[16:17]
	v_readfirstlane_b32 s24, v2
	s_cbranch_vccz .LBB0_197
	v_bfe_i32 v5, v2, 27, 1
	v_lshlrev_b32_e32 v3, 4, v2
	v_lshrrev_b32_e32 v5, 22, v5
	v_add_u32_e32 v5, v3, v5
	v_and_b32_e32 v5, 0xfffffc00, v5
	v_sub_u32_e32 v5, v3, v5
	v_ashrrev_i32_e32 v4, 31, v2
	v_lshrrev_b32_e32 v6, 4, v5
	v_lshrrev_b32_e32 v4, 26, v4
	v_bitop3_b32 v6, v6, v5, 32 bitop3:0x6c
	v_ashrrev_i32_e32 v5, 31, v5
	v_add_u32_e32 v4, v2, v4
	v_lshrrev_b32_e32 v5, 26, v5
	v_ashrrev_i32_e32 v4, 6, v4
	v_add_u32_e32 v5, v6, v5
	v_lshlrev_b32_e32 v7, 3, v4
	v_ashrrev_i32_e32 v5, 6, v5
	v_and_b32_e32 v7, -16, v7
	v_mul_i32_i24_e32 v8, 64, v5
	v_add_u32_e32 v7, v5, v7
	v_sub_u32_e32 v6, v6, v8
	v_mov_b32_e32 v8, 1
	v_lshlrev_b32_e32 v4, 5, v4
	v_ashrrev_i16_sdwa v6, v8, sext(v6) dst_sel:DWORD dst_unused:UNUSED_PAD src0_sel:DWORD src1_sel:BYTE_0
	v_lshlrev_b32_e32 v9, 1, v7
	v_lshrrev_b32_e32 v10, 2, v7
	v_and_b32_e32 v5, 3, v5
	s_mov_b32 s18, 0x1fffe0
	v_and_b32_e32 v4, 32, v4
	v_bfe_i32 v6, v6, 0, 16
	v_and_b32_e32 v9, 24, v9
	v_and_b32_e32 v10, 4, v10
	v_and_or_b32 v5, v7, s18, v5
	v_or3_b32 v5, v5, v10, v9
	v_add_lshl_u32 v4, v4, v6, 1
	v_add_u32_e32 v3, 0x2000, v3
	v_lshl_add_u32 v133, v7, 9, v4
	v_lshl_add_u32 v134, v5, 11, v4
	v_ashrrev_i32_e32 v4, 31, v3
	v_lshrrev_b32_e32 v4, 22, v4
	v_add_u32_e32 v4, v3, v4
	v_ashrrev_i32_e32 v4, 10, v4
	v_mul_i32_i24_e32 v5, 0x400, v4
	v_sub_u32_e32 v3, v3, v5
	v_lshrrev_b32_e32 v5, 4, v3
	v_bitop3_b32 v3, v5, v3, 32 bitop3:0x6c
	v_ashrrev_i32_e32 v6, 31, v3
	v_lshrrev_b32_e32 v6, 26, v6
	s_add_u32 s66, s4, 0x3400000
	v_lshlrev_b32_e32 v5, 3, v4
	v_add_u32_e32 v6, v3, v6
	s_addc_u32 s67, s5, 0
	v_and_b32_e32 v5, -16, v5
	v_ashrrev_i32_e32 v7, 6, v6
	v_and_b32_e32 v6, 0xc0, v6
	s_ashr_i32 s37, s24, 6
	s_ashr_i32 s25, s24, 8
	v_add_u32_e32 v5, v7, v5
	v_sub_u32_e32 v3, v3, v6
	s_lshl_b32 s27, s37, 10
	v_lshlrev_b32_e32 v4, 5, v4
	v_ashrrev_i16_sdwa v3, v8, sext(v3) dst_sel:DWORD dst_unused:UNUSED_PAD src0_sel:DWORD src1_sel:BYTE_0
	v_lshlrev_b32_e32 v6, 1, v5
	v_lshrrev_b32_e32 v8, 2, v5
	v_and_b32_e32 v7, 3, v7
	s_add_u32 s40, s66, s14
	v_and_b32_e32 v4, 32, v4
	v_bfe_i32 v3, v3, 0, 16
	v_and_b32_e32 v6, 24, v6
	v_and_b32_e32 v8, 4, v8
	v_and_or_b32 v7, v5, s18, v7
	s_addc_u32 s41, s67, s15
	s_add_i32 s26, s27, 0
	v_or3_b32 v6, v7, v8, v6
	v_add_lshl_u32 v3, v4, v3, 1
	s_add_i32 s28, s26, 0x10000
	s_mov_b32 s18, m0
	s_mov_b32 m0, s28
	s_nop 3
	global_load_lds_dwordx4 v134, s[40:41]
	s_mov_b32 m0, s18
	s_add_i32 s29, s26, 0x12000
	v_lshl_add_u32 v136, v6, 11, v3
	s_mov_b32 s18, m0
	s_mov_b32 m0, s29
	s_nop 3
	global_load_lds_dwordx4 v136, s[40:41]
	s_mov_b32 m0, s18
	s_add_u32 s20, s40, 0x40000
	s_addc_u32 s21, s41, 0
	s_add_i32 s30, s26, 0x14000
	s_mov_b32 s22, m0
	s_mov_b32 m0, s30
	s_nop 3
	global_load_lds_dwordx4 v134, s[20:21]
	s_mov_b32 m0, s22
	s_add_i32 s31, s26, 0x16000
	s_mov_b32 s22, m0
	s_mov_b32 m0, s31
	s_nop 3
	global_load_lds_dwordx4 v136, s[20:21]
	s_mov_b32 m0, s22
	s_mov_b32 s20, m0
	s_mov_b32 m0, s26
	s_nop 3
	global_load_lds_dwordx4 v133, s[8:9]
	s_mov_b32 m0, s20
	v_lshl_add_u32 v135, v5, 9, v3
	s_add_i32 s34, s26, 0x2000
	s_mov_b32 s20, m0
	s_mov_b32 m0, s34
	s_nop 3
	global_load_lds_dwordx4 v135, s[8:9]
	s_mov_b32 m0, s20
	s_add_i32 s35, s26, 0x4000
	s_mov_b32 s20, m0
	s_mov_b32 m0, s35
	s_nop 3
	global_load_lds_dwordx4 v133, s[12:13]
	s_mov_b32 m0, s20
	s_add_i32 s36, s26, 0x6000
	s_mov_b32 s22, m0
	s_mov_b32 m0, s36
	s_nop 3
	global_load_lds_dwordx4 v135, s[12:13]
	s_mov_b32 m0, s22
	s_cmp_eq_u32 s25, 1
	s_mov_b64 s[18:19], 0x40000
	s_cselect_b64 s[20:21], -1, 0
	s_cmp_lg_u32 s25, 1
	s_cbranch_scc1 .LBB0_184
	s_barrier
